# baseline (speedup 1.0000x reference)
.LBB0_11:
	s_andn2_b64 vcc, exec, s[4:5]
	s_cbranch_vccnz .LBB0_45
	s_load_dwordx4 s[32:35], s[0:1], 0x0
	s_load_dwordx2 s[36:37], s[0:1], 0x10
	v_lshlrev_b32_e32 v28, 2, v1
	s_cmpk_gt_u32 s2, 0x23f
	s_cbranch_scc0 .LBB0_18
	s_add_i32 s6, s3, 0xffffffb8
	s_mul_hi_u32 s7, s6, 0x88888889
	s_lshr_b32 s12, s7, 3
	s_mul_i32 s7, s12, 15
	s_sub_i32 s6, s6, s7
	s_and_b32 s7, s6, 0xff
	s_mulk_i32 s7, 0xcd
	s_lshr_b32 s13, s7, 10
	s_mul_i32 s7, s13, 5
	s_sub_i32 s14, s6, s7
	v_cmp_lt_u32_e32 vcc, 31, v0
	s_and_saveexec_b64 s[6:7], vcc
	s_xor_b64 s[6:7], exec, s[6:7]
	s_cbranch_execz .LBB0_26
	s_and_b32 s8, s14, 0xff
	s_cmp_lt_i32 s8, 1
	s_mov_b32 s15, 1
	s_cbranch_scc1 .LBB0_26
	s_and_b32 s9, 0xffff, s8
	s_cmp_lt_i32 s9, 2
	s_cbranch_scc1 .LBB0_19
	s_cmp_eq_u32 s9, 2
	s_cbranch_scc1 .LBB0_20
	s_cmp_eq_u32 s8, 3
	s_cselect_b32 s15, 5, 9
	s_mov_b64 s[8:9], 0
	s_branch .LBB0_21

.LBB0_42:
	v_cmp_gt_u32_e32 vcc, 9, v2
	s_movk_i32 s8, 0xe0
	v_mad_u32_u24 v6, v1, s8, v13
	v_cndmask_b32_e32 v2, 0, v2, vcc
	v_mad_u64_u32 v[14:15], s[6:7], v6, 9, v[2:3]
	v_mad_u32_u24 v6, v1, s8, v12
	v_mad_u64_u32 v[12:13], s[6:7], v6, 9, v[2:3]
	v_ashrrev_i32_e32 v13, 31, v12
	v_mad_u32_u24 v6, v1, s8, v9
	s_waitcnt lgkmcnt(0)
	global_load_dword v10, v28, s[34:35]
	global_load_dword v11, v28, s[36:37]
	v_lshl_add_u64 v[16:17], v[12:13], 2, s[32:33]
	v_mad_u64_u32 v[12:13], s[6:7], v6, 9, v[2:3]
	v_mad_u32_u24 v6, v1, s8, v8
	v_mad_u64_u32 v[8:9], s[6:7], v6, 9, v[2:3]
	v_mad_u32_u24 v6, v1, s8, v7
	v_mad_u64_u32 v[6:7], s[6:7], v6, 9, v[2:3]
	v_ashrrev_i32_e32 v7, 31, v6
	v_mad_u32_u24 v5, v1, s8, v5
	v_mad_u32_u24 v4, v1, s8, v4
	v_mad_u32_u24 v1, v1, s8, v3
	v_ashrrev_i32_e32 v15, 31, v14
	v_lshl_add_u64 v[22:23], v[6:7], 2, s[32:33]
	v_mad_u64_u32 v[6:7], s[6:7], v5, 9, v[2:3]
	v_mad_u64_u32 v[4:5], s[6:7], v4, 9, v[2:3]
	v_mad_u64_u32 v[2:3], s[6:7], v1, 9, v[2:3]
	v_lshl_add_u64 v[14:15], v[14:15], 2, s[32:33]
	v_ashrrev_i32_e32 v13, 31, v12
	v_ashrrev_i32_e32 v9, 31, v8
	v_ashrrev_i32_e32 v7, 31, v6
	v_ashrrev_i32_e32 v5, 31, v4
	v_ashrrev_i32_e32 v3, 31, v2
	v_lshl_add_u64 v[18:19], v[12:13], 2, s[32:33]
	v_lshl_add_u64 v[20:21], v[8:9], 2, s[32:33]
	v_lshl_add_u64 v[24:25], v[6:7], 2, s[32:33]
	v_lshl_add_u64 v[26:27], v[4:5], 2, s[32:33]
	v_lshl_add_u64 v[2:3], v[2:3], 2, s[32:33]
	global_load_dword v12, v[14:15], off
	global_load_dword v8, v[16:17], off
	global_load_dword v9, v[18:19], off
	global_load_dword v6, v[20:21], off
	global_load_dword v7, v[22:23], off
	global_load_dword v4, v[24:25], off
	global_load_dword v5, v[26:27], off
	global_load_dword v1, v[2:3], off
	s_and_b64 s[6:7], s[10:11], vcc
	v_mov_b32_e32 v3, 0
	v_mov_b32_e32 v2, 0
	s_and_saveexec_b64 s[4:5], s[6:7]
	s_cbranch_execz .LBB0_44
	s_waitcnt vmcnt(8)
	v_add_f32_e32 v2, 0x3727c5ac, v11
	s_mov_b32 s6, 0x800000
	v_mul_f32_e32 v11, 0x4b800000, v2
	v_cmp_gt_f32_e32 vcc, s6, v2
	s_nop 1
	v_cndmask_b32_e32 v2, v2, v11, vcc
	v_rsq_f32_e32 v2, v2
	s_nop 0
	v_mul_f32_e32 v11, 0x45800000, v2
	v_cndmask_b32_e32 v2, v2, v11, vcc
	v_mul_f32_e32 v2, v10, v2
